# speedup vs baseline: 1.0113x; 1.0062x over previous
_Z11lstm_kernel2LP:
	s_load_dword s37, s[0:1], 0x50
	s_load_dwordx16 s[8:23], s[0:1], 0x0
	s_add_u32 s26, s0, 0x50
	s_addc_u32 s27, s1, 0
	v_and_b32_e32 v162, 0x3ff, v0
	v_bfe_u32 v1, v0, 6, 4
	v_lshlrev_b32_e32 v137, 3, v1
	v_lshlrev_b32_e32 v163, 1, v162
	s_waitcnt lgkmcnt(0)
	s_and_b32 s3, s37, 31
	s_cmp_lg_u32 s3, 0
	s_cbranch_scc0 .Lmap_xcd
	s_lshr_b32 s51, s2, 2
	s_and_b32 s34, s2, 3
	s_and_b32 s6, s51, 1
	s_branch .Lmap_done
.Lmap_xcd:
	s_and_b32 s0, s2, 7
	s_lshr_b32 s1, s2, 3
	s_and_b32 s34, s1, 3
	s_lshr_b32 s1, s1, 2
	s_lshl_b32 s51, s1, 3
	s_or_b32 s51, s51, s0
	s_add_i32 s6, s0, s1
	s_and_b32 s6, s6, 1
.Lmap_done:
	s_mov_b32 s7, 32
	s_cmp_eq_u32 s6, 0
	v_bfe_u32 v2, v0, 2, 8
	s_cselect_b64 s[0:1], -1, 0
	v_lshl_or_b32 v2, v162, 8, v2
	s_movk_i32 s4, 0x303
	s_and_b64 s[2:3], s[0:1], exec
	v_and_or_b32 v4, v2, s4, v137
	v_mov_b32_e32 v212, 0
	s_cselect_b32 s3, s11, s13
	s_cselect_b32 s2, s10, s12
	v_and_b32_e32 v2, 0x60, v163
	v_mov_b32_e32 v3, v212
	v_lshlrev_b32_e32 v4, 10, v4
	v_lshl_add_u64 v[2:3], s[2:3], 0, v[2:3]
	v_lshl_or_b32 v4, s34, 16, v4
	v_mov_b32_e32 v5, v212
	v_lshl_add_u64 v[208:209], v[2:3], 0, v[4:5]
	s_mov_b64 s[4:5], 0x1000
	s_lshl_b32 s10, s51, 5
	s_add_u32 s10, s20, s10
	s_addc_u32 s11, s21, 0
	v_lshl_add_u64 v[210:211], v[208:209], 0, s[4:5]
	v_cmp_eq_u32_e64 s[2:3], 0, v162
	s_and_saveexec_b64 s[12:13], s[2:3]
	s_cbranch_execz .Larr1
	s_getreg_b32 s5, hwreg(HW_REG_XCC_ID, 0, 4)
	s_and_b32 s5, s5, 15
	s_lshl_b32 s20, s34, 2
	s_add_i32 s20, s20, 4
	s_lshl_b32 s5, s5, s20
	s_or_b32 s5, s5, 1
	v_mov_b32_e32 v213, 0
	v_mov_b32_e32 v214, s5
	global_atomic_add v215, v213, v214, s[10:11] sc0
.Larr1:
	s_or_b64 exec, exec, s[12:13]
	global_load_dwordx4 v[6:9], v[208:209], off offset:896
	global_load_dwordx4 v[10:13], v[208:209], off offset:912
	global_load_dwordx4 v[14:17], v[210:211], off offset:896
	global_load_dwordx4 v[18:21], v[210:211], off offset:912
	global_load_dwordx4 v[22:25], v[208:209], off
	global_load_dwordx4 v[26:29], v[208:209], off offset:16
	global_load_dwordx4 v[30:33], v[208:209], off offset:128
	global_load_dwordx4 v[34:37], v[208:209], off offset:144
	global_load_dwordx4 v[38:41], v[208:209], off offset:256
	global_load_dwordx4 v[42:45], v[208:209], off offset:272
	global_load_dwordx4 v[46:49], v[208:209], off offset:384
	global_load_dwordx4 v[50:53], v[208:209], off offset:400
	global_load_dwordx4 v[54:57], v[208:209], off offset:512
	global_load_dwordx4 v[58:61], v[208:209], off offset:528
	global_load_dwordx4 v[62:65], v[208:209], off offset:640
	global_load_dwordx4 v[66:69], v[208:209], off offset:656
	global_load_dwordx4 v[70:73], v[208:209], off offset:768
	global_load_dwordx4 v[74:77], v[208:209], off offset:784
	global_load_dwordx4 v[78:81], v[210:211], off
	global_load_dwordx4 v[82:85], v[210:211], off offset:16
	global_load_dwordx4 v[86:89], v[210:211], off offset:128
	global_load_dwordx4 v[90:93], v[210:211], off offset:144
	global_load_dwordx4 v[94:97], v[210:211], off offset:256
	global_load_dwordx4 v[98:101], v[210:211], off offset:272
	global_load_dwordx4 v[102:105], v[210:211], off offset:384
	global_load_dwordx4 v[106:109], v[210:211], off offset:400
	global_load_dwordx4 v[110:113], v[210:211], off offset:512
	global_load_dwordx4 v[114:117], v[210:211], off offset:528
	global_load_dwordx4 v[118:121], v[210:211], off offset:640
	global_load_dwordx4 v[122:125], v[210:211], off offset:656
	global_load_dwordx4 v[126:129], v[210:211], off offset:768
	global_load_dwordx4 v[130:133], v[210:211], off offset:784
	s_and_saveexec_b64 s[12:13], s[2:3]
	s_cbranch_execz .Larr2
	s_waitcnt vmcnt(32)
	v_and_b32_e32 v215, 7, v215
	v_cmp_eq_u32_e32 vcc, 3, v215
	s_cbranch_vccz .Larr2
	s_lshl_b32 s20, s6, 2
	v_mov_b32_e32 v213, s20
	v_mov_b32_e32 v214, 1
	global_atomic_add v215, v213, v214, s[22:23] offset:12 sc0
	s_waitcnt vmcnt(0)
	v_add_u32_e32 v215, 1, v215
	v_lshlrev_b32_e32 v215, 24, v215
	v_mov_b32_e32 v213, 0
	global_atomic_add v213, v215, s[10:11]
.Larr2:
	s_or_b64 exec, exec, s[12:13]
	s_mov_b32 s36, 0x43800000
	s_waitcnt vmcnt(30)
	v_fma_mixlo_f16 v2, v6, s36, 0
	v_fma_mixhi_f16 v2, v7, s36, 0
	v_fma_mixlo_f16 v3, v8, s36, 0
	v_fma_mixhi_f16 v3, v9, s36, 0
	v_fma_mixlo_f16 v4, v10, s36, 0
	v_fma_mixhi_f16 v4, v11, s36, 0
	v_fma_mixlo_f16 v5, v12, s36, 0
	v_fma_mixhi_f16 v5, v13, s36, 0
	v_fma_mixlo_f16 v6, v6, s36, -v2 op_sel_hi:[0,0,1]
	v_fma_mixhi_f16 v6, v7, s36, -v2 op_sel:[0,0,1] op_sel_hi:[0,0,1]
	v_fma_mixlo_f16 v7, v8, s36, -v3 op_sel_hi:[0,0,1]
	v_fma_mixhi_f16 v7, v9, s36, -v3 op_sel:[0,0,1] op_sel_hi:[0,0,1]
	v_fma_mixlo_f16 v8, v10, s36, -v4 op_sel_hi:[0,0,1]
	v_fma_mixhi_f16 v8, v11, s36, -v4 op_sel:[0,0,1] op_sel_hi:[0,0,1]
	v_fma_mixlo_f16 v9, v12, s36, -v5 op_sel_hi:[0,0,1]
	v_fma_mixhi_f16 v9, v13, s36, -v5 op_sel:[0,0,1] op_sel_hi:[0,0,1]
	s_waitcnt vmcnt(28)
	v_fma_mixlo_f16 v10, v14, s36, 0
	v_fma_mixhi_f16 v10, v15, s36, 0
	v_fma_mixlo_f16 v11, v16, s36, 0
	v_fma_mixhi_f16 v11, v17, s36, 0
	v_fma_mixlo_f16 v12, v18, s36, 0
	v_fma_mixhi_f16 v12, v19, s36, 0
	v_fma_mixlo_f16 v13, v20, s36, 0
	v_fma_mixhi_f16 v13, v21, s36, 0
	v_fma_mixlo_f16 v14, v14, s36, -v10 op_sel_hi:[0,0,1]
	v_fma_mixhi_f16 v14, v15, s36, -v10 op_sel:[0,0,1] op_sel_hi:[0,0,1]
	v_fma_mixlo_f16 v15, v16, s36, -v11 op_sel_hi:[0,0,1]
	v_fma_mixhi_f16 v15, v17, s36, -v11 op_sel:[0,0,1] op_sel_hi:[0,0,1]
	v_fma_mixlo_f16 v16, v18, s36, -v12 op_sel_hi:[0,0,1]
	v_fma_mixhi_f16 v16, v19, s36, -v12 op_sel:[0,0,1] op_sel_hi:[0,0,1]
	v_fma_mixlo_f16 v17, v20, s36, -v13 op_sel_hi:[0,0,1]
	v_fma_mixhi_f16 v17, v21, s36, -v13 op_sel:[0,0,1] op_sel_hi:[0,0,1]
	s_waitcnt vmcnt(26)
	v_fma_mixlo_f16 v18, v22, s36, 0
	v_fma_mixhi_f16 v18, v23, s36, 0
	v_fma_mixlo_f16 v19, v24, s36, 0
	v_fma_mixhi_f16 v19, v25, s36, 0
	v_fma_mixlo_f16 v20, v26, s36, 0
	v_fma_mixhi_f16 v20, v27, s36, 0
	v_fma_mixlo_f16 v21, v28, s36, 0
	v_fma_mixhi_f16 v21, v29, s36, 0
	v_fma_mixlo_f16 v22, v22, s36, -v18 op_sel_hi:[0,0,1]
	v_fma_mixhi_f16 v22, v23, s36, -v18 op_sel:[0,0,1] op_sel_hi:[0,0,1]
	v_fma_mixlo_f16 v23, v24, s36, -v19 op_sel_hi:[0,0,1]
	v_fma_mixhi_f16 v23, v25, s36, -v19 op_sel:[0,0,1] op_sel_hi:[0,0,1]
	v_fma_mixlo_f16 v24, v26, s36, -v20 op_sel_hi:[0,0,1]
	v_fma_mixhi_f16 v24, v27, s36, -v20 op_sel:[0,0,1] op_sel_hi:[0,0,1]
	v_fma_mixlo_f16 v25, v28, s36, -v21 op_sel_hi:[0,0,1]
	v_fma_mixhi_f16 v25, v29, s36, -v21 op_sel:[0,0,1] op_sel_hi:[0,0,1]
	s_waitcnt vmcnt(24)
	v_fma_mixlo_f16 v26, v30, s36, 0
	v_fma_mixhi_f16 v26, v31, s36, 0
	v_fma_mixlo_f16 v27, v32, s36, 0
	v_fma_mixhi_f16 v27, v33, s36, 0
	v_fma_mixlo_f16 v28, v34, s36, 0
	v_fma_mixhi_f16 v28, v35, s36, 0
	v_fma_mixlo_f16 v29, v36, s36, 0
	v_fma_mixhi_f16 v29, v37, s36, 0
	v_fma_mixlo_f16 v30, v30, s36, -v26 op_sel_hi:[0,0,1]
	v_fma_mixhi_f16 v30, v31, s36, -v26 op_sel:[0,0,1] op_sel_hi:[0,0,1]
	v_fma_mixlo_f16 v31, v32, s36, -v27 op_sel_hi:[0,0,1]
	v_fma_mixhi_f16 v31, v33, s36, -v27 op_sel:[0,0,1] op_sel_hi:[0,0,1]
	v_fma_mixlo_f16 v32, v34, s36, -v28 op_sel_hi:[0,0,1]
	v_fma_mixhi_f16 v32, v35, s36, -v28 op_sel:[0,0,1] op_sel_hi:[0,0,1]
	v_fma_mixlo_f16 v33, v36, s36, -v29 op_sel_hi:[0,0,1]
	v_fma_mixhi_f16 v33, v37, s36, -v29 op_sel:[0,0,1] op_sel_hi:[0,0,1]
	s_waitcnt vmcnt(22)
	v_fma_mixlo_f16 v34, v38, s36, 0
	v_fma_mixhi_f16 v34, v39, s36, 0
	v_fma_mixlo_f16 v35, v40, s36, 0
	v_fma_mixhi_f16 v35, v41, s36, 0
	v_fma_mixlo_f16 v36, v42, s36, 0
	v_fma_mixhi_f16 v36, v43, s36, 0
	v_fma_mixlo_f16 v37, v44, s36, 0
	v_fma_mixhi_f16 v37, v45, s36, 0
	v_fma_mixlo_f16 v38, v38, s36, -v34 op_sel_hi:[0,0,1]
	v_fma_mixhi_f16 v38, v39, s36, -v34 op_sel:[0,0,1] op_sel_hi:[0,0,1]
	v_fma_mixlo_f16 v39, v40, s36, -v35 op_sel_hi:[0,0,1]
	v_fma_mixhi_f16 v39, v41, s36, -v35 op_sel:[0,0,1] op_sel_hi:[0,0,1]
	v_fma_mixlo_f16 v40, v42, s36, -v36 op_sel_hi:[0,0,1]
	v_fma_mixhi_f16 v40, v43, s36, -v36 op_sel:[0,0,1] op_sel_hi:[0,0,1]
	v_fma_mixlo_f16 v41, v44, s36, -v37 op_sel_hi:[0,0,1]
	v_fma_mixhi_f16 v41, v45, s36, -v37 op_sel:[0,0,1] op_sel_hi:[0,0,1]
	s_waitcnt vmcnt(20)
	v_fma_mixlo_f16 v42, v46, s36, 0
	v_fma_mixhi_f16 v42, v47, s36, 0
	v_fma_mixlo_f16 v43, v48, s36, 0
	v_fma_mixhi_f16 v43, v49, s36, 0
	v_fma_mixlo_f16 v44, v50, s36, 0
	v_fma_mixhi_f16 v44, v51, s36, 0
	v_fma_mixlo_f16 v45, v52, s36, 0
	v_fma_mixhi_f16 v45, v53, s36, 0
	v_fma_mixlo_f16 v46, v46, s36, -v42 op_sel_hi:[0,0,1]
	v_fma_mixhi_f16 v46, v47, s36, -v42 op_sel:[0,0,1] op_sel_hi:[0,0,1]
	v_fma_mixlo_f16 v47, v48, s36, -v43 op_sel_hi:[0,0,1]
	v_fma_mixhi_f16 v47, v49, s36, -v43 op_sel:[0,0,1] op_sel_hi:[0,0,1]
	v_fma_mixlo_f16 v48, v50, s36, -v44 op_sel_hi:[0,0,1]
	v_fma_mixhi_f16 v48, v51, s36, -v44 op_sel:[0,0,1] op_sel_hi:[0,0,1]
	v_fma_mixlo_f16 v49, v52, s36, -v45 op_sel_hi:[0,0,1]
	v_fma_mixhi_f16 v49, v53, s36, -v45 op_sel:[0,0,1] op_sel_hi:[0,0,1]
	s_waitcnt vmcnt(18)
	v_fma_mixlo_f16 v50, v54, s36, 0
	v_fma_mixhi_f16 v50, v55, s36, 0
	v_fma_mixlo_f16 v51, v56, s36, 0
	v_fma_mixhi_f16 v51, v57, s36, 0
	v_fma_mixlo_f16 v52, v58, s36, 0
	v_fma_mixhi_f16 v52, v59, s36, 0
	v_fma_mixlo_f16 v53, v60, s36, 0
	v_fma_mixhi_f16 v53, v61, s36, 0
	v_fma_mixlo_f16 v54, v54, s36, -v50 op_sel_hi:[0,0,1]
	v_fma_mixhi_f16 v54, v55, s36, -v50 op_sel:[0,0,1] op_sel_hi:[0,0,1]
	v_fma_mixlo_f16 v55, v56, s36, -v51 op_sel_hi:[0,0,1]
	v_fma_mixhi_f16 v55, v57, s36, -v51 op_sel:[0,0,1] op_sel_hi:[0,0,1]
	v_fma_mixlo_f16 v56, v58, s36, -v52 op_sel_hi:[0,0,1]
	v_fma_mixhi_f16 v56, v59, s36, -v52 op_sel:[0,0,1] op_sel_hi:[0,0,1]
	v_fma_mixlo_f16 v57, v60, s36, -v53 op_sel_hi:[0,0,1]
	v_fma_mixhi_f16 v57, v61, s36, -v53 op_sel:[0,0,1] op_sel_hi:[0,0,1]
	s_waitcnt vmcnt(16)
	v_fma_mixlo_f16 v58, v62, s36, 0
	v_fma_mixhi_f16 v58, v63, s36, 0
	v_fma_mixlo_f16 v59, v64, s36, 0
	v_fma_mixhi_f16 v59, v65, s36, 0
	v_fma_mixlo_f16 v60, v66, s36, 0
	v_fma_mixhi_f16 v60, v67, s36, 0
	v_fma_mixlo_f16 v61, v68, s36, 0
	v_fma_mixhi_f16 v61, v69, s36, 0
	v_fma_mixlo_f16 v62, v62, s36, -v58 op_sel_hi:[0,0,1]
	v_fma_mixhi_f16 v62, v63, s36, -v58 op_sel:[0,0,1] op_sel_hi:[0,0,1]
	v_fma_mixlo_f16 v63, v64, s36, -v59 op_sel_hi:[0,0,1]
	v_fma_mixhi_f16 v63, v65, s36, -v59 op_sel:[0,0,1] op_sel_hi:[0,0,1]
	v_fma_mixlo_f16 v64, v66, s36, -v60 op_sel_hi:[0,0,1]
	v_fma_mixhi_f16 v64, v67, s36, -v60 op_sel:[0,0,1] op_sel_hi:[0,0,1]
	v_fma_mixlo_f16 v65, v68, s36, -v61 op_sel_hi:[0,0,1]
	v_fma_mixhi_f16 v65, v69, s36, -v61 op_sel:[0,0,1] op_sel_hi:[0,0,1]
	s_waitcnt vmcnt(14)
	v_fma_mixlo_f16 v66, v70, s36, 0
	v_fma_mixhi_f16 v66, v71, s36, 0
	v_fma_mixlo_f16 v67, v72, s36, 0
	v_fma_mixhi_f16 v67, v73, s36, 0
	v_fma_mixlo_f16 v68, v74, s36, 0
	v_fma_mixhi_f16 v68, v75, s36, 0
	v_fma_mixlo_f16 v69, v76, s36, 0
	v_fma_mixhi_f16 v69, v77, s36, 0
	v_fma_mixlo_f16 v70, v70, s36, -v66 op_sel_hi:[0,0,1]
	v_fma_mixhi_f16 v70, v71, s36, -v66 op_sel:[0,0,1] op_sel_hi:[0,0,1]
	v_fma_mixlo_f16 v71, v72, s36, -v67 op_sel_hi:[0,0,1]
	v_fma_mixhi_f16 v71, v73, s36, -v67 op_sel:[0,0,1] op_sel_hi:[0,0,1]
	v_fma_mixlo_f16 v72, v74, s36, -v68 op_sel_hi:[0,0,1]
	v_fma_mixhi_f16 v72, v75, s36, -v68 op_sel:[0,0,1] op_sel_hi:[0,0,1]
	v_fma_mixlo_f16 v73, v76, s36, -v69 op_sel_hi:[0,0,1]
	v_fma_mixhi_f16 v73, v77, s36, -v69 op_sel:[0,0,1] op_sel_hi:[0,0,1]
	s_waitcnt vmcnt(12)
	v_fma_mixlo_f16 v74, v78, s36, 0
	v_fma_mixhi_f16 v74, v79, s36, 0
	v_fma_mixlo_f16 v75, v80, s36, 0
	v_fma_mixhi_f16 v75, v81, s36, 0
	v_fma_mixlo_f16 v76, v82, s36, 0
	v_fma_mixhi_f16 v76, v83, s36, 0
	v_fma_mixlo_f16 v77, v84, s36, 0
	v_fma_mixhi_f16 v77, v85, s36, 0
	v_fma_mixlo_f16 v78, v78, s36, -v74 op_sel_hi:[0,0,1]
	v_fma_mixhi_f16 v78, v79, s36, -v74 op_sel:[0,0,1] op_sel_hi:[0,0,1]
	v_fma_mixlo_f16 v79, v80, s36, -v75 op_sel_hi:[0,0,1]
	v_fma_mixhi_f16 v79, v81, s36, -v75 op_sel:[0,0,1] op_sel_hi:[0,0,1]
	v_fma_mixlo_f16 v80, v82, s36, -v76 op_sel_hi:[0,0,1]
	v_fma_mixhi_f16 v80, v83, s36, -v76 op_sel:[0,0,1] op_sel_hi:[0,0,1]
	v_fma_mixlo_f16 v81, v84, s36, -v77 op_sel_hi:[0,0,1]
	v_fma_mixhi_f16 v81, v85, s36, -v77 op_sel:[0,0,1] op_sel_hi:[0,0,1]
	s_waitcnt vmcnt(10)
	v_fma_mixlo_f16 v82, v86, s36, 0
	v_fma_mixhi_f16 v82, v87, s36, 0
	v_fma_mixlo_f16 v83, v88, s36, 0
	v_fma_mixhi_f16 v83, v89, s36, 0
	v_fma_mixlo_f16 v84, v90, s36, 0
	v_fma_mixhi_f16 v84, v91, s36, 0
	v_fma_mixlo_f16 v85, v92, s36, 0
	v_fma_mixhi_f16 v85, v93, s36, 0
	v_fma_mixlo_f16 v86, v86, s36, -v82 op_sel_hi:[0,0,1]
	v_fma_mixhi_f16 v86, v87, s36, -v82 op_sel:[0,0,1] op_sel_hi:[0,0,1]
	v_fma_mixlo_f16 v87, v88, s36, -v83 op_sel_hi:[0,0,1]
	v_fma_mixhi_f16 v87, v89, s36, -v83 op_sel:[0,0,1] op_sel_hi:[0,0,1]
	v_fma_mixlo_f16 v88, v90, s36, -v84 op_sel_hi:[0,0,1]
	v_fma_mixhi_f16 v88, v91, s36, -v84 op_sel:[0,0,1] op_sel_hi:[0,0,1]
	v_fma_mixlo_f16 v89, v92, s36, -v85 op_sel_hi:[0,0,1]
	v_fma_mixhi_f16 v89, v93, s36, -v85 op_sel:[0,0,1] op_sel_hi:[0,0,1]
	s_waitcnt vmcnt(8)
	v_fma_mixlo_f16 v90, v94, s36, 0
	v_fma_mixhi_f16 v90, v95, s36, 0
	v_fma_mixlo_f16 v91, v96, s36, 0
	v_fma_mixhi_f16 v91, v97, s36, 0
	v_fma_mixlo_f16 v92, v98, s36, 0
	v_fma_mixhi_f16 v92, v99, s36, 0
	v_fma_mixlo_f16 v93, v100, s36, 0
	v_fma_mixhi_f16 v93, v101, s36, 0
	v_fma_mixlo_f16 v94, v94, s36, -v90 op_sel_hi:[0,0,1]
	v_fma_mixhi_f16 v94, v95, s36, -v90 op_sel:[0,0,1] op_sel_hi:[0,0,1]
	v_fma_mixlo_f16 v95, v96, s36, -v91 op_sel_hi:[0,0,1]
	v_fma_mixhi_f16 v95, v97, s36, -v91 op_sel:[0,0,1] op_sel_hi:[0,0,1]
	v_fma_mixlo_f16 v96, v98, s36, -v92 op_sel_hi:[0,0,1]
	v_fma_mixhi_f16 v96, v99, s36, -v92 op_sel:[0,0,1] op_sel_hi:[0,0,1]
	v_fma_mixlo_f16 v97, v100, s36, -v93 op_sel_hi:[0,0,1]
	v_fma_mixhi_f16 v97, v101, s36, -v93 op_sel:[0,0,1] op_sel_hi:[0,0,1]
	s_waitcnt vmcnt(6)
	v_fma_mixlo_f16 v98, v102, s36, 0
	v_fma_mixhi_f16 v98, v103, s36, 0
	v_fma_mixlo_f16 v99, v104, s36, 0
	v_fma_mixhi_f16 v99, v105, s36, 0
	v_fma_mixlo_f16 v100, v106, s36, 0
	v_fma_mixhi_f16 v100, v107, s36, 0
	v_fma_mixlo_f16 v101, v108, s36, 0
	v_fma_mixhi_f16 v101, v109, s36, 0
	v_fma_mixlo_f16 v102, v102, s36, -v98 op_sel_hi:[0,0,1]
	v_fma_mixhi_f16 v102, v103, s36, -v98 op_sel:[0,0,1] op_sel_hi:[0,0,1]
	v_fma_mixlo_f16 v103, v104, s36, -v99 op_sel_hi:[0,0,1]
	v_fma_mixhi_f16 v103, v105, s36, -v99 op_sel:[0,0,1] op_sel_hi:[0,0,1]
	v_fma_mixlo_f16 v104, v106, s36, -v100 op_sel_hi:[0,0,1]
	v_fma_mixhi_f16 v104, v107, s36, -v100 op_sel:[0,0,1] op_sel_hi:[0,0,1]
	v_fma_mixlo_f16 v105, v108, s36, -v101 op_sel_hi:[0,0,1]
	v_fma_mixhi_f16 v105, v109, s36, -v101 op_sel:[0,0,1] op_sel_hi:[0,0,1]
	s_waitcnt vmcnt(4)
	v_fma_mixlo_f16 v106, v110, s36, 0
	v_fma_mixhi_f16 v106, v111, s36, 0
	v_fma_mixlo_f16 v107, v112, s36, 0
	v_fma_mixhi_f16 v107, v113, s36, 0
	v_fma_mixlo_f16 v108, v114, s36, 0
	v_fma_mixhi_f16 v108, v115, s36, 0
	v_fma_mixlo_f16 v109, v116, s36, 0
	v_fma_mixhi_f16 v109, v117, s36, 0
	v_fma_mixlo_f16 v110, v110, s36, -v106 op_sel_hi:[0,0,1]
	v_fma_mixhi_f16 v110, v111, s36, -v106 op_sel:[0,0,1] op_sel_hi:[0,0,1]
	v_fma_mixlo_f16 v111, v112, s36, -v107 op_sel_hi:[0,0,1]
	v_fma_mixhi_f16 v111, v113, s36, -v107 op_sel:[0,0,1] op_sel_hi:[0,0,1]
	v_fma_mixlo_f16 v112, v114, s36, -v108 op_sel_hi:[0,0,1]
	v_fma_mixhi_f16 v112, v115, s36, -v108 op_sel:[0,0,1] op_sel_hi:[0,0,1]
	v_fma_mixlo_f16 v113, v116, s36, -v109 op_sel_hi:[0,0,1]
	v_fma_mixhi_f16 v113, v117, s36, -v109 op_sel:[0,0,1] op_sel_hi:[0,0,1]
	s_waitcnt vmcnt(2)
	v_fma_mixlo_f16 v114, v118, s36, 0
	v_fma_mixhi_f16 v114, v119, s36, 0
	v_fma_mixlo_f16 v115, v120, s36, 0
	v_fma_mixhi_f16 v115, v121, s36, 0
	v_fma_mixlo_f16 v116, v122, s36, 0
	v_fma_mixhi_f16 v116, v123, s36, 0
	v_fma_mixlo_f16 v117, v124, s36, 0
	v_fma_mixhi_f16 v117, v125, s36, 0
	v_fma_mixlo_f16 v118, v118, s36, -v114 op_sel_hi:[0,0,1]
	v_fma_mixhi_f16 v118, v119, s36, -v114 op_sel:[0,0,1] op_sel_hi:[0,0,1]
	v_fma_mixlo_f16 v119, v120, s36, -v115 op_sel_hi:[0,0,1]
	v_fma_mixhi_f16 v119, v121, s36, -v115 op_sel:[0,0,1] op_sel_hi:[0,0,1]
	v_fma_mixlo_f16 v120, v122, s36, -v116 op_sel_hi:[0,0,1]
	v_fma_mixhi_f16 v120, v123, s36, -v116 op_sel:[0,0,1] op_sel_hi:[0,0,1]
	v_fma_mixlo_f16 v121, v124, s36, -v117 op_sel_hi:[0,0,1]
	v_fma_mixhi_f16 v121, v125, s36, -v117 op_sel:[0,0,1] op_sel_hi:[0,0,1]
	s_waitcnt vmcnt(0)
	v_fma_mixlo_f16 v122, v126, s36, 0
	v_fma_mixhi_f16 v122, v127, s36, 0
	v_fma_mixlo_f16 v123, v128, s36, 0
	v_fma_mixhi_f16 v123, v129, s36, 0
	v_fma_mixlo_f16 v124, v130, s36, 0
	v_fma_mixhi_f16 v124, v131, s36, 0
	v_fma_mixlo_f16 v125, v132, s36, 0
	v_fma_mixhi_f16 v125, v133, s36, 0
	v_fma_mixlo_f16 v126, v126, s36, -v122 op_sel_hi:[0,0,1]
	v_fma_mixhi_f16 v126, v127, s36, -v122 op_sel:[0,0,1] op_sel_hi:[0,0,1]
	v_fma_mixlo_f16 v127, v128, s36, -v123 op_sel_hi:[0,0,1]
	v_fma_mixhi_f16 v127, v129, s36, -v123 op_sel:[0,0,1] op_sel_hi:[0,0,1]
	v_fma_mixlo_f16 v128, v130, s36, -v124 op_sel_hi:[0,0,1]
	v_fma_mixhi_f16 v128, v131, s36, -v124 op_sel:[0,0,1] op_sel_hi:[0,0,1]
	v_fma_mixlo_f16 v129, v132, s36, -v125 op_sel_hi:[0,0,1]
	v_fma_mixhi_f16 v129, v133, s36, -v125 op_sel:[0,0,1] op_sel_hi:[0,0,1]
	v_mov_b32_e32 v212, 0
	s_mov_b32 s28, 0
.Ltk_poll:
	global_load_dword v214, v212, s[10:11] sc1
	s_waitcnt vmcnt(0)
	v_readfirstlane_b32 s20, v214
	s_lshr_b32 s21, s20, 24
	s_cmp_lg_u32 s21, 0
	s_cbranch_scc1 .Ltk_got
	s_add_i32 s28, s28, 1
	s_and_b32 s5, s28, 0x3ff
	s_cmp_lg_u32 s5, 0
	s_cbranch_scc1 .Ltk_poll
	s_cmp_gt_u32 s28, 0x80000
	s_cbranch_scc1 .Ltk_dead
	global_load_dword v215, v212, s[22:23] offset:4 sc1
	s_waitcnt vmcnt(0)
	v_readfirstlane_b32 s5, v215
	s_cmp_eq_u32 s5, 0
	s_cbranch_scc1 .Ltk_poll
.Ltk_dead:
	v_mov_b32_e32 v215, 1
	global_store_dword v212, v215, s[22:23] offset:4 sc1
	s_lshl_b32 s40, s6, 5
	s_add_i32 s24, s40, 31
	v_mov_b32_e32 v1, 1
	s_branch .LBB1_169
.Ltk_got:
	s_add_i32 s41, s21, -1
	s_cmp_lt_u32 s41, 16
	s_cselect_b32 s46, 5, 4
	s_cmp_lt_u32 s41, 28
	s_cselect_b32 s46, s46, 0
	s_mul_i32 s12, s41, 5
	s_lshl_b32 s13, s41, 2
	s_add_i32 s13, s13, 16
	s_cmp_lt_u32 s41, 17
	s_cselect_b32 s48, s12, s13
	s_lshl_b32 s48, s48, 4
	s_add_i32 s47, s46, 31
	s_add_i32 s49, s46, 32
	s_add_i32 s4, s41, -1
	s_cmp_lt_u32 s4, 16
	s_cselect_b32 s50, 5, 4
	s_cmp_lt_u32 s4, 28
	s_cselect_b32 s50, s50, 0
	s_add_i32 s50, s50, 32
	s_cmp_eq_u32 s41, 0
	s_cselect_b32 s50, s49, s50
	s_lshl_b32 s40, s6, 5
	s_add_i32 s24, s40, s41
	s_ashr_i32 s25, s24, 31
	s_lshr_b32 s4, s20, 4
	s_lshr_b32 s5, s20, 8
	s_xor_b32 s4, s4, s5
	s_and_b32 s4, s4, 0xfff
	s_cmp_eq_u32 s4, 0
	s_cselect_b64 s[20:21], -1, 0
	s_mov_b64 s[10:11], 0
	s_cmp_eq_u32 s46, 0
	s_cbranch_scc0 .Ltk_work
	v_mov_b32_e32 v1, 0
	s_branch .LBB1_169
.Ltk_work:
	v_add_u32_e32 v165, 0xfffffe00, v162
	s_movk_i32 s5, 0x1eff
	v_mov_b32_e32 v213, v163
	v_mov_b32_e32 v215, v165
	s_mov_b64 s[12:13], 0
.LBB1_16:
	v_add_u32_e32 v215, 0x200, v215
	v_cmp_lt_u32_e32 vcc, s5, v215
	ds_write_b16 v213, v212
	s_or_b64 s[12:13], vcc, s[12:13]
	v_add_u32_e32 v213, 0x400, v213
	s_andn2_b64 exec, exec, s[12:13]
	s_cbranch_execnz .LBB1_16
	s_or_b64 exec, exec, s[12:13]
	s_waitcnt lgkmcnt(0)
	s_barrier
	v_readfirstlane_b32 s4, v162
	s_bitcmp1_b32 s4, 8
	s_cbranch_scc0 .Lnoprio
	s_setprio 1
.Lnoprio:
	s_lshl_b64 s[28:29], s[24:25], 16
	s_add_u32 s33, s16, s28
	s_addc_u32 s35, s17, s29
	s_mul_i32 s40, s6, s7
	s_ashr_i32 s7, s6, 31
	s_sub_i32 s41, s24, s40
	s_lshl_b64 s[4:5], s[6:7], 23
	s_add_u32 s4, s8, s4
	s_addc_u32 s5, s9, s5
	s_lshl_b32 s8, s34, 8
	s_lshl_b32 s9, s34, 10
	s_add_u32 s28, s4, s9
	s_addc_u32 s29, s5, 0
	s_lshl_b64 s[4:5], s[6:7], 21
	s_add_u32 s4, s14, s4
	s_addc_u32 s5, s15, s5
	s_lshl_b32 s42, s34, 6
	s_add_u32 s30, s4, s8
	s_addc_u32 s31, s5, 0
	v_and_b32_e32 v171, 15, v162
	s_lshl_b32 s4, s41, 6
	v_mul_u32_u24_e32 v130, s46, v171
	v_add_u32_e32 v130, s48, v130
	v_subrev_u32_e32 v201, 32, v130
	v_max_i32_e32 v130, 0, v201
	v_sub_u32_e32 v131, 0x7ff, v130
	v_cndmask_b32_e64 v130, v131, v130, s[0:1]
	v_bfe_u32 v146, v162, 4, 2
	v_ashrrev_i32_e32 v131, 31, v130
	v_or_b32_e32 v199, v137, v146
	v_lshlrev_b64 v[130:131], 12, v[130:131]
	v_or_b32_e32 v134, 4, v199
	v_lshl_add_u64 v[130:131], s[28:29], 0, v[130:131]
	v_mov_b32_e32 v167, 0
	v_lshlrev_b32_e32 v166, 4, v199
	v_lshl_add_u64 v[132:133], v[130:131], 0, v[166:167]
	v_lshlrev_b32_e32 v166, 4, v134
	v_lshl_add_u64 v[130:131], v[130:131], 0, v[166:167]
	global_load_dwordx4 v[142:145], v[130:131], off
	global_load_dwordx4 v[138:141], v[132:133], off
	v_lshlrev_b32_e32 v164, 2, v199
	v_lshlrev_b32_e32 v170, 2, v134
	v_lshlrev_b32_e32 v134, 8, v171
	s_mov_b32 s4, 0x8400
	v_add3_u32 v203, v134, v164, s4
	v_lshlrev_b32_e32 v134, 1, v1
	v_sub_u32_e32 v135, v134, v171
	v_or_b32_e32 v134, 1, v134
	v_sub_u32_e32 v134, v134, v171
	s_lshl_b32 s4, s34, 4
	v_mul_lo_u32 v206, v134, s46
	v_mul_u32_u24_e32 v134, 6, v1
	s_add_i32 s4, s4, 16
	v_mad_u32_u24 v130, v1, 6, s4
	v_and_b32_e32 v131, 14, v134
	v_and_or_b32 v130, v130, 48, v131
	v_lshlrev_b32_e32 v172, 6, v130
	v_or_b32_e32 v130, 1, v134
	v_add_u32_e32 v130, s4, v130
	v_bitop3_b32 v131, v134, 15, 1 bitop3:0xc8
	v_and_or_b32 v130, v130, 48, v131
	v_lshlrev_b32_e32 v174, 6, v130
	v_mad_u32_u24 v130, v1, 6, 2
	v_add_u32_e32 v131, s4, v130
	v_and_b32_e32 v132, 14, v130
	v_and_or_b32 v131, v131, 48, v132
	v_lshlrev_b32_e32 v176, 6, v131
	v_mad_u32_u24 v131, v1, 6, 3
	v_and_b32_e32 v136, 63, v162
	v_add_u32_e32 v132, s4, v131
	v_and_b32_e32 v133, 15, v131
	v_lshlrev_b32_e32 v166, 2, v136
	v_and_or_b32 v132, v132, 48, v133
	v_mul_lo_u32 v204, v135, s46
	v_lshl_or_b32 v135, v1, 9, v166
	v_lshlrev_b32_e32 v178, 6, v132
	v_mad_u32_u24 v132, v1, 6, 4
	v_add_u32_e32 v205, 0x8400, v135
	v_add_u32_e32 v133, s4, v132
	v_and_b32_e32 v135, 14, v132
	v_and_or_b32 v133, v133, 48, v135
	s_add_i32 s34, s34, 1
	v_lshrrev_b32_e32 v134, 4, v134
	v_lshl_add_u32 v184, v1, 7, s9
	v_lshlrev_b32_e32 v180, 6, v133
	v_mad_u32_u24 v133, v1, 6, 5
	v_add_lshl_u32 v134, s34, v134, 6
	v_mul_u32_u24_e32 v1, 24, v1
	v_and_b32_e32 v134, 0xc0, v134
	v_and_b32_e32 v1, 56, v1
	v_or3_b32 v183, v1, v134, v146
	v_lshrrev_b32_e32 v1, 4, v130
	v_add_lshl_u32 v1, s34, v1, 6
	v_lshlrev_b32_e32 v130, 2, v130
	v_and_b32_e32 v1, 0xc0, v1
	v_and_b32_e32 v130, 56, v130
	v_or3_b32 v185, v130, v1, v146
	v_lshrrev_b32_e32 v1, 4, v131
	v_add_lshl_u32 v1, s34, v1, 6
	v_lshlrev_b32_e32 v130, 2, v131
	v_and_b32_e32 v1, 0xc0, v1
	v_and_b32_e32 v130, 60, v130
	v_or3_b32 v192, v130, v1, v146
	v_lshrrev_b32_e32 v1, 4, v132
	v_add_lshl_u32 v1, s34, v1, 6
	v_lshlrev_b32_e32 v130, 2, v132
	v_and_b32_e32 v1, 0xc0, v1
	v_and_b32_e32 v130, 56, v130
	v_or3_b32 v193, v130, v1, v146
	v_lshrrev_b32_e32 v1, 4, v133
	v_add_u32_e32 v135, s4, v133
	v_and_b32_e32 v137, 15, v133
	v_add_lshl_u32 v1, s34, v1, 6
	v_lshlrev_b32_e32 v130, 2, v133
	v_and_or_b32 v135, v135, 48, v137
	v_and_b32_e32 v1, 0xc0, v1
	v_and_b32_e32 v130, 60, v130
	v_lshlrev_b32_e32 v182, 6, v135
	v_or3_b32 v194, v130, v1, v146
	v_lshlrev_b32_e32 v168, 3, v136
	s_waitcnt vmcnt(1)
	v_mov_b64_e32 v[130:131], v[142:143]
	s_waitcnt vmcnt(0)
	v_mov_b64_e32 v[134:135], v[138:139]
	s_mov_b32 s43, 0
	v_lshlrev_b32_e32 v173, 3, v146
	v_and_b32_e32 v200, 48, v162
	v_add_u32_e32 v181, s42, v199
	s_mov_b32 s34, 0x48800000
	s_mov_b32 s36, 0x36800000
	v_mov_b32_e32 v188, v167
	v_mov_b32_e32 v189, v167
	v_mul_u32_u24_e32 v195, 0x210, v171
	v_bfe_u32 v216, v162, 4, 1
	v_bfe_u32 v217, v162, 5, 1
	s_lshr_b32 s4, s42, 6
	s_add_i32 s4, s4, 1
	v_lshlrev_b32_e32 v218, 3, v171
	v_lshrrev_b32_e32 v219, 6, v162
	v_mad_u32_u24 v219, v219, 6, v217
	v_lshrrev_b32_e32 v220, 4, v219
	v_add_u32_e32 v220, s4, v220
	v_and_b32_e32 v220, 3, v220
	v_and_b32_e32 v221, 15, v219
	v_lshl_add_u32 v222, v220, 4, v221
	v_lshlrev_b32_e32 v223, 6, v222
	v_lshl_add_u32 v223, v216, 5, v223
	v_lshl_add_u32 v228, v223, 3, v218
	v_lshlrev_b32_e32 v223, 2, v222
	v_lshl_add_u32 v223, v216, 1, v223
	v_lshl_add_u32 v231, v223, 1, v195
	v_add_u32_e32 v219, 2, v219
	v_lshrrev_b32_e32 v220, 4, v219
	v_add_u32_e32 v220, s4, v220
	v_and_b32_e32 v220, 3, v220
	v_and_b32_e32 v221, 15, v219
	v_lshl_add_u32 v222, v220, 4, v221
	v_lshlrev_b32_e32 v223, 6, v222
	v_lshl_add_u32 v223, v216, 5, v223
	v_lshl_add_u32 v229, v223, 3, v218
	v_lshlrev_b32_e32 v223, 2, v222
	v_lshl_add_u32 v223, v216, 1, v223
	v_lshl_add_u32 v232, v223, 1, v195
	v_add_u32_e32 v219, 2, v219
	v_lshrrev_b32_e32 v220, 4, v219
	v_add_u32_e32 v220, s4, v220
	v_and_b32_e32 v220, 3, v220
	v_and_b32_e32 v221, 15, v219
	v_lshl_add_u32 v222, v220, 4, v221
	v_lshlrev_b32_e32 v223, 6, v222
	v_lshl_add_u32 v223, v216, 5, v223
	v_lshl_add_u32 v230, v223, 3, v218
	v_lshlrev_b32_e32 v223, 2, v222
	v_lshl_add_u32 v223, v216, 1, v223
	v_lshl_add_u32 v233, v223, 1, v195
	v_lshl_add_u32 v234, v184, 3, v168
	v_mov_b32_e32 v207, 1
	v_mov_b32_e32 v202, 0
	v_mov_b32_e32 v198, 0
	v_mov_b32_e32 v197, 0
	v_mov_b32_e32 v196, 0
	v_mov_b32_e32 v179, 0
	v_mov_b32_e32 v177, 0
	v_mov_b32_e32 v175, 0
	v_mov_b32_e32 v1, 0
	v_lshl_add_u64 v[186:187], s[30:31], 0, v[166:167]
	v_mov_b64_e32 v[132:133], v[144:145]
	v_mov_b64_e32 v[136:137], v[140:141]
.LBB1_20:
	s_cmp_lg_u32 s43, s47
	s_cselect_b64 s[4:5], -1, 0
	s_cmp_eq_u32 s43, s47
	v_add_u32_e32 v190, s43, v201
.LBB1_22:
	s_and_b32 s12, s43, 1
	s_cmp_lt_u32 s43, 24
	s_mul_i32 s8, s12, 0x4200
	s_mov_b64 s[6:7], -1
	s_cbranch_scc1 .LBB1_24
	v_lshlrev_b32_e32 v146, 1, v173
	v_add3_u32 v166, s8, v195, v146
	ds_read_b128 v[146:149], v166
	ds_read_b128 v[150:153], v166 offset:64
	ds_read_b128 v[212:215], v166 offset:8448
	ds_read_b128 v[216:219], v166 offset:8512
	s_cmp_eq_u32 s43, s47
	s_cbranch_scc1 .Lx_skip_f
	v_max_i32_e32 v130, -1, v190
	v_add_u32_e32 v131, 1, v130
	v_sub_u32_e32 v130, 0x7fe, v130
	v_cndmask_b32_e64 v130, v130, v131, s[0:1]
	v_lshlrev_b32_e32 v130, 12, v130
	v_lshl_add_u32 v226, v164, 2, v130
	global_load_dwordx4 v[134:137], v226, s[28:29]
	global_load_dwordx4 v[130:133], v226, s[28:29] offset:64

.LBB1_24:
	s_andn2_b64 vcc, exec, s[6:7]
	s_cbranch_vccnz .LBB1_26
	v_add3_u32 v166, s8, v195, v200
	s_nop 3
	ds_read_b128 v[146:149], v166
	ds_read_b128 v[150:153], v166 offset:64
	ds_read_b128 v[154:157], v166 offset:128
	ds_read_b128 v[158:161], v166 offset:192
	ds_read_b128 v[208:211], v166 offset:256
	ds_read_b128 v[212:215], v166 offset:320
	ds_read_b128 v[216:219], v166 offset:384
	ds_read_b128 v[220:223], v166 offset:448
	s_cmp_eq_u32 s43, s47
	s_cbranch_scc1 .Lx_skip_l
	v_max_i32_e32 v130, -1, v190
	v_add_u32_e32 v131, 1, v130
	v_sub_u32_e32 v130, 0x7fe, v130
	v_cndmask_b32_e64 v130, v130, v131, s[0:1]
	v_lshlrev_b32_e32 v130, 12, v130
	v_lshl_add_u32 v226, v164, 2, v130
	global_load_dwordx4 v[134:137], v226, s[28:29]
	global_load_dwordx4 v[130:133], v226, s[28:29] offset:64

.LBB1_53:
	s_cmp_eq_u32 s43, 32
	s_cselect_b64 vcc, -1, 0
	v_cndmask_b32_e32 v1, v1, v139, vcc
	v_cndmask_b32_e32 v175, v175, v138, vcc
	s_cmp_eq_u32 s44, s49
	s_waitcnt lgkmcnt(0)
	s_barrier
	s_cbranch_scc1 .LBB1_55
	s_waitcnt vmcnt(1)
	v_mov_b64_e32 v[140:141], v[136:137]
	s_waitcnt vmcnt(0)
	v_mov_b64_e32 v[144:145], v[132:133]
	s_mov_b32 s43, s44
	v_mov_b64_e32 v[138:139], v[134:135]
	v_mov_b64_e32 v[142:143], v[130:131]
	s_branch .LBB1_20
.LBB1_55:
	s_xor_b64 s[10:11], s[10:11], -1
	s_lshl_b64 s[4:5], s[24:25], 15
	s_add_u32 s6, s18, s4
	s_addc_u32 s7, s19, s5
	s_waitcnt vmcnt(0)
	v_lshlrev_b32_e32 v130, 11, v171
	s_mov_b32 s4, 0
	v_mov_b32_e32 v131, 0
	v_lshl_add_u64 v[132:133], s[6:7], 0, v[130:131]
	s_lshl_b32 s6, s42, 3
	s_mov_b32 s7, s4
	v_lshl_add_u64 v[132:133], v[132:133], 0, s[6:7]
	v_lshlrev_b32_e32 v130, 3, v199
	s_cmp_gt_i32 s41, 0
	v_lshl_add_u64 v[132:133], v[132:133], 0, v[130:131]
	v_mov_b32_e32 v135, 1
	v_mov_b32_e32 v134, v188
	s_cselect_b64 s[8:9], -1, 0
	global_store_dwordx2 v[132:133], v[134:135], off sc1
	v_mov_b32_e32 v134, v189
	s_and_b64 s[12:13], s[8:9], exec
	global_store_dwordx2 v[132:133], v[134:135], off offset:32 sc1
	s_cselect_b32 s5, 15, 0
	v_add_co_u32_e32 v133, vcc, -1, v171
	v_mov_b32_e32 v132, s5
	s_or_b64 s[8:9], vcc, s[8:9]
	v_cndmask_b32_e32 v132, v132, v133, vcc
	v_mov_b32_e32 v133, s24
	s_xor_b64 vcc, vcc, s[8:9]
	v_subbrev_co_u32_e32 v134, vcc, 0, v133, vcc
	v_ashrrev_i32_e32 v135, 31, v134
	v_lshlrev_b64 v[136:137], 16, v[134:135]
	v_lshl_add_u64 v[136:137], s[16:17], 0, v[136:137]
	v_ashrrev_i32_e32 v133, 31, v132
	v_lshl_add_u64 v[136:137], v[132:133], 3, v[136:137]
	v_mov_b32_e32 v224, s49
	v_mov_b32_e32 v225, s50
	v_cmp_eq_u32_e32 vcc, 0, v171
	v_mov_b32_e32 v227, 0
	s_nop 0
	v_cndmask_b32_e32 v224, v224, v225, vcc
	v_and_b32_e32 v226, 1, v224
	v_lshlrev_b32_e32 v226, 15, v226
	v_lshl_add_u64 v[136:137], v[136:137], 0, v[226:227]
	v_mov_b32_e32 v139, 0
	v_lshlrev_b32_e32 v208, 3, v171
	v_sub_u32_e32 v138, v228, v208
	v_lshl_add_u64 v[140:141], v[136:137], 0, v[138:139]
	v_sub_u32_e32 v138, v229, v208
	v_lshl_add_u64 v[144:145], v[136:137], 0, v[138:139]
	v_sub_u32_e32 v138, v230, v208
	v_lshl_add_u64 v[148:149], v[136:137], 0, v[138:139]
	v_lshlrev_b64 v[134:135], 15, v[134:135]
	v_lshl_add_u64 v[134:135], s[18:19], 0, v[134:135]
	v_lshlrev_b64 v[132:133], 11, v[132:133]
	v_lshl_add_u64 v[132:133], v[134:135], 0, v[132:133]
	v_lshl_add_u64 v[132:133], v[132:133], 0, s[6:7]
	v_lshl_add_u64 v[152:153], v[132:133], 0, v[130:131]
	v_mov_b32_e32 v208, 0
	v_mov_b32_e32 v210, 0
	v_mov_b32_e32 v212, 0
	v_mov_b32_e32 v214, 0
	v_mov_b32_e32 v216, 0
	v_mov_b32_e32 v218, 0
	v_mov_b32_e32 v220, 0
	v_mov_b32_e32 v222, 0
	s_mov_b32 s12, 1
	s_andn2_b64 vcc, exec, s[10:11]
	s_cbranch_vccnz .Lep_check
	s_mov_b32 s7, 0
.Lep_poll:
	global_load_dwordx2 v[208:209], v[140:141], off sc1
	global_load_dwordx2 v[210:211], v[140:141], off offset:128 sc1
	global_load_dwordx2 v[212:213], v[144:145], off sc1
	global_load_dwordx2 v[214:215], v[144:145], off offset:128 sc1
	global_load_dwordx2 v[216:217], v[148:149], off sc1
	global_load_dwordx2 v[218:219], v[148:149], off offset:128 sc1
	global_load_dwordx2 v[220:221], v[152:153], off sc1
	global_load_dwordx2 v[222:223], v[152:153], off offset:32 sc1
	s_waitcnt vmcnt(0)
	v_cmp_eq_u32_e32 vcc, v224, v209
	v_cmp_eq_u32_e64 s[14:15], v224, v211
	v_cmp_eq_u32_e64 s[16:17], v224, v213
	s_and_b64 vcc, vcc, s[14:15]
	v_cmp_eq_u32_e64 s[14:15], v224, v215
	s_and_b64 vcc, vcc, s[16:17]
	v_cmp_eq_u32_e64 s[16:17], v224, v217
	s_and_b64 vcc, vcc, s[14:15]
	v_cmp_eq_u32_e64 s[14:15], v224, v219
	s_and_b64 vcc, vcc, s[16:17]
	v_cmp_eq_u32_e64 s[16:17], 1, v221
	s_and_b64 vcc, vcc, s[14:15]
	v_cmp_eq_u32_e64 s[14:15], 1, v223
	s_and_b64 vcc, vcc, s[16:17]
	s_and_b64 vcc, vcc, s[14:15]
	s_cmp_eq_u64 vcc, exec
	s_cbranch_scc1 .Lep_ok
	s_add_i32 s7, s7, 1
	s_and_b32 s13, s7, 0x3ff
	s_cmp_lg_u32 s13, 0
	s_cbranch_scc1 .Lep_poll
	s_cmp_gt_u32 s7, 0x80000
	s_cbranch_scc1 .Lep_dead
	v_mov_b32_e32 v138, 0
	global_load_dword v139, v138, s[22:23] offset:4 sc1
	s_waitcnt vmcnt(0)
	v_cmp_eq_u32_e64 s[14:15], 0, v139
	s_and_b64 vcc, exec, s[14:15]
	s_cbranch_vccnz .Lep_poll
